# baseline (speedup 1.0000x reference)
.LBB5_203:
	v_lshrrev_b32_e32 v81, 4, v0
	v_lshlrev_b32_e32 v79, 2, v81
	s_waitcnt lgkmcnt(0)
	global_load_dword v80, v79, s[4:5]
	s_lshr_b32 s4, s30, 2
	s_and_b32 s4, s4, 0x3ffffff0
	v_lshrrev_b32_e32 v77, 5, v0
	v_and_or_b32 v66, v77, 1, s4
	v_mov_b32_e32 v67, 0
	v_and_b32_e32 v1, 0x400, v1
	v_lshlrev_b64 v[2:3], 17, v[66:67]
	v_lshl_or_b32 v4, s15, 11, v1
	v_and_b32_e32 v1, 32, v76
	v_lshl_add_u64 v[2:3], s[2:3], 0, v[2:3]
	v_ashrrev_i32_e32 v5, 31, v4
	v_lshlrev_b32_e32 v1, 2, v1
	v_and_b32_e32 v78, 7, v0
	v_lshl_add_u64 v[2:3], v[4:5], 2, v[2:3]
	v_lshl_or_b32 v4, s14, 8, v1
	v_mov_b32_e32 v5, v67
	v_lshl_add_u64 v[2:3], v[2:3], 0, v[4:5]
	v_lshlrev_b32_e32 v4, 4, v78
	v_lshl_add_u64 v[2:3], v[2:3], 0, v[4:5]
	s_mov_b32 s2, 0x40000
	v_add_co_u32_e64 v4, s[2:3], s2, v2
	s_lshl_b32 s16, s15, 8
	s_nop 0
	v_addc_co_u32_e64 v5, s[2:3], 0, v3, s[2:3]
	s_mov_b32 s2, 0x80000
	global_load_dwordx4 v[54:57], v[2:3], off nt
	global_load_dwordx4 v[50:53], v[4:5], off nt
	v_add_co_u32_e64 v4, s[2:3], s2, v2
	s_lshl_b32 s17, s14, 4
	s_nop 0
	v_addc_co_u32_e64 v5, s[2:3], 0, v3, s[2:3]
	s_mov_b32 s2, 0xc0000
	s_nop 0
	v_add_co_u32_e64 v6, s[2:3], s2, v2
	s_or_b32 s16, s16, s17
	s_nop 0
	v_addc_co_u32_e64 v7, s[2:3], 0, v3, s[2:3]
	s_mov_b32 s2, 0x100000
	global_load_dwordx4 v[46:49], v[4:5], off nt
	global_load_dwordx4 v[42:45], v[6:7], off nt
	v_add_co_u32_e64 v4, s[2:3], s2, v2
	v_or_b32_e32 v70, s16, v77
	s_nop 0
	v_addc_co_u32_e64 v5, s[2:3], 0, v3, s[2:3]
	s_mov_b32 s2, 0x140000
	s_nop 0
	v_add_co_u32_e64 v6, s[2:3], s2, v2
	v_ashrrev_i32_e32 v71, 31, v70
	s_nop 0
	v_addc_co_u32_e64 v7, s[2:3], 0, v3, s[2:3]
	s_mov_b32 s2, 0x180000
	global_load_dwordx4 v[34:37], v[4:5], off nt
	global_load_dwordx4 v[26:29], v[6:7], off nt
	v_add_co_u32_e64 v4, s[2:3], s2, v2
	v_lshlrev_b64 v[6:7], 9, v[70:71]
	s_nop 0
	v_addc_co_u32_e64 v5, s[2:3], 0, v3, s[2:3]
	s_mov_b32 s2, 0x1c0000
	v_and_b32_e32 v1, 0x7c, v76
	v_add_co_u32_e64 v2, s[2:3], s2, v2
	v_lshl_add_u64 v[6:7], s[12:13], 0, v[6:7]
	v_lshlrev_b32_e32 v74, 2, v1
	v_mov_b32_e32 v75, v67
	v_addc_co_u32_e64 v3, s[2:3], 0, v3, s[2:3]
	v_lshl_add_u64 v[6:7], v[6:7], 0, v[74:75]
	global_load_dwordx4 v[38:41], v[4:5], off nt
	global_load_dwordx4 v[30:33], v[2:3], off nt
	global_load_dwordx4 v[22:25], v[6:7], off nt
	global_load_dwordx4 v[10:13], v74, s[6:7]
	global_load_dwordx4 v[14:17], v74, s[10:11]
	v_lshlrev_b32_e32 v71, 2, v78
	v_bfe_u32 v75, v0, 3, 4
	s_cmpk_lt_u32 s30, 0x80
	s_cselect_b64 s[2:3], -1, 0
	s_cmpk_gt_u32 s30, 0x7f
	v_mov_b32_e32 v7, v67
	v_mov_b32_e32 v2, v67
	v_mov_b32_e32 v3, v67
	v_mov_b32_e32 v18, v67
	v_mov_b32_e32 v19, v67
	v_mov_b32_e32 v8, v67
	v_mov_b32_e32 v9, v67
	v_mov_b32_e32 v4, v67
	v_mov_b32_e32 v5, v67
	v_mov_b32_e32 v20, v67
	v_mov_b32_e32 v21, v67
	v_or_b32_e32 v68, s16, v75
	v_lshlrev_b32_e32 v72, 2, v71
	s_cbranch_scc1 .LBB5_226
	s_load_dwordx2 s[10:11], s[0:1], 0x18
	s_load_dwordx4 s[4:7], s[0:1], 0x40
	v_ashrrev_i32_e32 v69, 31, v68
	v_lshlrev_b64 v[2:3], 7, v[68:69]
	v_mov_b32_e32 v73, 0
	s_waitcnt lgkmcnt(0)
	v_lshl_add_u64 v[2:3], s[10:11], 0, v[2:3]
	v_lshl_add_u64 v[82:83], v[2:3], 0, v[72:73]
	global_load_dwordx4 v[2:5], v72, s[4:5]
	global_load_dwordx4 v[6:9], v72, s[6:7]
	global_load_dwordx4 v[18:21], v[82:83], off nt
	v_lshlrev_b32_e32 v99, 2, v76
	s_and_saveexec_b64 s[4:5], vcc
	s_cbranch_execnz .LBB5_227

.LBB5_206:
	s_waitcnt vmcnt(12)
	ds_write_b128 v99, v[58:61] offset:14080
.LBB5_207:
	v_and_b32_e32 v99, 15, v0
	v_lshlrev_b32_e32 v73, 3, v99
	v_add_u32_e32 v76, 0x2800, v73
	s_waitcnt lgkmcnt(0)
	s_barrier
	v_mul_u32_u24_e32 v69, 0xe0, v81
	s_waitcnt vmcnt(12)
	ds_read2_b64 v[58:61], v76 offset0:32 offset1:48
	ds_read_b128 v[62:65], v69 offset:14080
	ds_read_b128 v[82:85], v69 offset:14096
	ds_read_b128 v[86:89], v69 offset:14112
	ds_read_b128 v[90:93], v69 offset:14128
	ds_read2_b64 v[94:97], v76 offset0:64 offset1:80
	v_and_b32_e32 v98, 24, v0
	v_add_u32_e32 v73, 0x3000, v73
	s_waitcnt lgkmcnt(4)
	v_mul_f32_e32 v0, v59, v63
	v_fmac_f32_e32 v0, v58, v62
	v_mul_f32_e32 v58, v61, v65
	s_waitcnt vmcnt(11)
	v_add_f32_e32 v0, v80, v0
	v_fmac_f32_e32 v58, v60, v64
	s_waitcnt lgkmcnt(0)
	v_mul_f32_e32 v62, v95, v83
	v_add_f32_e32 v0, v0, v58
	v_fmac_f32_e32 v62, v94, v82
	ds_read2_b64 v[58:61], v76 offset0:96 offset1:112
	v_add_f32_e32 v0, v0, v62
	v_mul_f32_e32 v62, v97, v85
	v_fmac_f32_e32 v62, v96, v84
	v_add_f32_e32 v0, v0, v62
	ds_read2_b64 v[62:65], v76 offset0:128 offset1:144
	s_waitcnt lgkmcnt(1)
	v_mul_f32_e32 v59, v59, v87
	v_fmac_f32_e32 v59, v58, v86
	v_mul_f32_e32 v58, v61, v89
	v_add_f32_e32 v0, v0, v59
	v_fmac_f32_e32 v58, v60, v88
	v_add_f32_e32 v0, v0, v58
	s_waitcnt lgkmcnt(0)
	v_mul_f32_e32 v58, v63, v91
	v_fmac_f32_e32 v58, v62, v90
	v_add_f32_e32 v0, v0, v58
	ds_read2_b64 v[58:61], v76 offset0:160 offset1:176
	ds_read_b128 v[80:83], v69 offset:14144
	v_mul_f32_e32 v62, v65, v93
	v_fmac_f32_e32 v62, v64, v92
	v_add_f32_e32 v0, v0, v62
	ds_read_b128 v[62:65], v69 offset:14160
	ds_read2_b64 v[84:87], v76 offset0:192 offset1:208
	s_waitcnt lgkmcnt(2)
	v_mul_f32_e32 v59, v59, v81
	v_fmac_f32_e32 v59, v58, v80
	v_mul_f32_e32 v58, v61, v83
	v_add_f32_e32 v0, v0, v59
	v_fmac_f32_e32 v58, v60, v82
	v_add_f32_e32 v0, v0, v58
	s_waitcnt lgkmcnt(0)
	v_mul_f32_e32 v58, v85, v63
	v_fmac_f32_e32 v58, v84, v62
	v_add_f32_e32 v0, v0, v58
	ds_read2_b64 v[58:61], v76 offset0:224 offset1:240
	ds_read_b128 v[80:83], v69 offset:14176
	v_mul_f32_e32 v62, v87, v65
	v_fmac_f32_e32 v62, v86, v64
	v_add_f32_e32 v0, v0, v62
	ds_read_b128 v[62:65], v69 offset:14192
	ds_read2_b64 v[84:87], v73 offset1:16
	s_waitcnt lgkmcnt(2)
	v_mul_f32_e32 v59, v59, v81
	v_fmac_f32_e32 v59, v58, v80
	v_mul_f32_e32 v58, v61, v83
	v_add_f32_e32 v0, v0, v59
	v_fmac_f32_e32 v58, v60, v82
	v_add_f32_e32 v0, v0, v58
	ds_read_b128 v[80:83], v69 offset:14224
	s_waitcnt lgkmcnt(1)
	v_mul_f32_e32 v58, v85, v63
	v_fmac_f32_e32 v58, v84, v62
	v_mul_f32_e32 v76, v87, v65
	v_add_f32_e32 v0, v0, v58
	ds_read_b128 v[58:61], v69 offset:14208
	v_fmac_f32_e32 v76, v86, v64
	ds_read2_b64 v[62:65], v73 offset0:32 offset1:48
	v_add_f32_e32 v0, v0, v76
	s_movk_i32 s4, 0x290
	s_waitcnt lgkmcnt(1)
	v_mov_b32_e32 v84, v59
	v_mov_b32_e32 v59, v61
	s_waitcnt lgkmcnt(0)
	v_pk_mov_b32 v[86:87], v[62:63], v[64:65] op_sel:[1,0]
	v_mov_b32_e32 v63, v65
	v_mov_b32_e32 v85, v60
	v_pk_mul_f32 v[58:59], v[62:63], v[58:59]
	s_waitcnt vmcnt(10)
	v_add_f32_e32 v54, v54, v55
	v_pk_fma_f32 v[62:63], v[86:87], v[84:85], v[58:59]
	ds_read2_b64 v[58:61], v73 offset0:64 offset1:80
	v_add_f32_e32 v0, v0, v62
	v_mov_b32_e32 v62, v81
	v_mov_b32_e32 v81, v83
	v_add_f32_e32 v0, v0, v63
	s_waitcnt lgkmcnt(0)
	v_pk_mov_b32 v[64:65], v[58:59], v[60:61] op_sel:[1,0]
	v_mov_b32_e32 v59, v61
	v_mov_b32_e32 v63, v82
	v_pk_mul_f32 v[58:59], v[58:59], v[80:81]
	v_add_f32_e32 v56, v56, v57
	v_pk_fma_f32 v[80:81], v[64:65], v[62:63], v[58:59]
	ds_read_b128 v[58:61], v69 offset:14240
	ds_read2_b64 v[62:65], v73 offset0:96 offset1:112
	v_add_f32_e32 v0, v0, v80
	v_add_f32_e32 v0, v0, v81
	ds_read_b128 v[80:83], v69 offset:14256
	s_waitcnt lgkmcnt(2)
	v_mov_b32_e32 v84, v59
	s_waitcnt lgkmcnt(1)
	v_pk_mov_b32 v[86:87], v[62:63], v[64:65] op_sel:[1,0]
	v_mov_b32_e32 v63, v65
	v_mov_b32_e32 v59, v61
	v_mov_b32_e32 v85, v60
	v_pk_mul_f32 v[58:59], v[62:63], v[58:59]
	s_nop 0
	v_pk_fma_f32 v[62:63], v[86:87], v[84:85], v[58:59]
	ds_read2_b64 v[58:61], v73 offset0:128 offset1:144
	v_add_f32_e32 v0, v0, v62
	s_waitcnt lgkmcnt(1)
	v_mov_b32_e32 v62, v81
	v_mov_b32_e32 v81, v83
	v_add_f32_e32 v0, v0, v63
	s_waitcnt lgkmcnt(0)
	v_pk_mov_b32 v[64:65], v[58:59], v[60:61] op_sel:[1,0]
	v_mov_b32_e32 v59, v61
	v_mov_b32_e32 v63, v82
	v_pk_mul_f32 v[58:59], v[58:59], v[80:81]
	s_nop 0
	v_pk_fma_f32 v[80:81], v[64:65], v[62:63], v[58:59]
	ds_read_b128 v[58:61], v69 offset:14272
	ds_read2_b64 v[62:65], v73 offset0:160 offset1:176
	v_add_f32_e32 v0, v0, v80
	v_add_f32_e32 v0, v0, v81
	ds_read_b128 v[80:83], v69 offset:14288
	s_waitcnt lgkmcnt(2)
	v_mov_b32_e32 v84, v59
	s_waitcnt lgkmcnt(1)
	v_pk_mov_b32 v[86:87], v[62:63], v[64:65] op_sel:[1,0]
	v_mov_b32_e32 v63, v65
	v_mov_b32_e32 v59, v61
	v_mov_b32_e32 v85, v60
	v_pk_mul_f32 v[58:59], v[62:63], v[58:59]
	s_nop 0
	v_pk_fma_f32 v[62:63], v[86:87], v[84:85], v[58:59]
	ds_read2_b64 v[58:61], v73 offset0:192 offset1:208
	v_add_f32_e32 v0, v0, v62
	s_waitcnt lgkmcnt(1)
	v_mov_b32_e32 v62, v81
	v_mov_b32_e32 v81, v83
	v_add_f32_e32 v0, v0, v63
	s_waitcnt lgkmcnt(0)
	v_pk_mov_b32 v[64:65], v[58:59], v[60:61] op_sel:[1,0]
	v_mov_b32_e32 v59, v61
	v_mov_b32_e32 v63, v82
	v_pk_mul_f32 v[58:59], v[58:59], v[80:81]
	s_nop 0
	v_pk_fma_f32 v[58:59], v[64:65], v[62:63], v[58:59]
	v_mad_u32_u24 v62, v99, s4, v79
	v_add_f32_e32 v0, v0, v58
	v_add_f32_e32 v61, v0, v59
	v_mbcnt_lo_u32_b32 v0, -1, 0
	v_mbcnt_hi_u32_b32 v58, -1, v0
	v_and_b32_e32 v99, 64, v58
	v_xor_b32_e32 v0, 8, v58
	v_add_u32_e32 v59, 64, v99
	v_cmp_lt_i32_e32 vcc, v0, v59
	ds_write_b32 v62, v61 offset:512
	s_nop 0
	v_cndmask_b32_e32 v0, v58, v0, vcc
	v_lshlrev_b32_e32 v99, 2, v0
	v_xor_b32_e32 v0, 16, v58
	v_cmp_lt_i32_e32 vcc, v0, v59
	s_nop 1
	v_add_f32_dpp v55, v54, v54 row_ror:8 row_mask:0xf bank_mask:0xf
	v_cndmask_b32_e32 v0, v58, v0, vcc
	v_lshlrev_b32_e32 v0, 2, v0
	v_add_f32_dpp v56, v56, v56 row_ror:8 row_mask:0xf bank_mask:0xf
	v_mov_b32_e32 v57, v55
	v_mov_b32_e32 v60, v56
	s_nop 1
	v_permlane16_swap_b32_e32 v57, v55
	v_permlane16_swap_b32_e32 v60, v56
	v_mul_u32_u24_e32 v54, 0x520, v78
	v_cmp_eq_u32_e32 vcc, 0, v98
	v_lshl_add_u32 v54, v66, 2, v54
	s_and_saveexec_b64 s[4:5], vcc
	s_cbranch_execz .LBB5_209
	v_add_f32_e32 v56, v56, v60
	v_add_f32_e32 v55, v55, v57
	v_mul_f32_e32 v55, 0x3e000000, v55
	v_mul_f32_e32 v56, 0x3e000000, v56
	ds_write2_b32 v54, v55, v56 offset1:164

.LBB5_223:
	s_or_b64 exec, exec, s[0:1]
	s_movk_i32 s6, 0x290
	v_mad_u32_u24 v26, v77, s6, v74
	s_waitcnt lgkmcnt(0)
	s_barrier
	ds_read_b128 v[28:31], v26
	v_xor_b32_e32 v26, 1, v58
	v_cmp_lt_i32_e32 vcc, v26, v59
	s_mov_b32 s8, 0xf800000
	s_movk_i32 s7, 0x140
	s_waitcnt vmcnt(2) lgkmcnt(0)
	v_pk_add_f32 v[28:29], v[22:23], v[28:29]
	v_pk_add_f32 v[30:31], v[24:25], v[30:31]
	v_add_f32_e32 v22, v28, v29
	v_cndmask_b32_e32 v26, v58, v26, vcc
	v_add_f32_e32 v22, v22, v30
	v_lshlrev_b32_e32 v26, 2, v26
	v_add_f32_e32 v22, v22, v31
	s_nop 1
	v_mov_b32_dpp v24, v22 quad_perm:[1,0,3,2] row_mask:0xf bank_mask:0xf
	v_xor_b32_e32 v23, 2, v58
	v_cmp_lt_i32_e32 vcc, v23, v59
	s_waitcnt lgkmcnt(0)
	v_add_f32_e32 v22, v22, v24
	v_cndmask_b32_e32 v23, v58, v23, vcc
	v_lshlrev_b32_e32 v23, 2, v23
	s_nop 1
	v_mov_b32_dpp v25, v22 quad_perm:[2,3,0,1] row_mask:0xf bank_mask:0xf
	v_xor_b32_e32 v24, 4, v58
	v_cmp_lt_i32_e32 vcc, v24, v59
	s_waitcnt lgkmcnt(0)
	v_add_f32_e32 v22, v22, v25
	v_cndmask_b32_e32 v24, v58, v24, vcc
	v_lshlrev_b32_e32 v24, 2, v24
	s_nop 1
	v_mov_b32_dpp v25, v22 row_half_mirror row_mask:0xf bank_mask:0xf
	s_waitcnt lgkmcnt(0)
	v_add_f32_e32 v22, v22, v25
	s_nop 1
	v_mov_b32_dpp v25, v22 row_mirror row_mask:0xf bank_mask:0xf
	s_waitcnt lgkmcnt(0)
	v_add_f32_e32 v22, v22, v25
	v_mov_b32_e32 v25, v22
	s_nop 1
	v_permlane16_swap_b32_e32 v22, v25
	s_waitcnt lgkmcnt(0)
	v_add_f32_e32 v22, v22, v25
	v_mul_f32_e32 v22, 0x3c000000, v22
	v_pk_add_f32 v[28:29], v[28:29], v[22:23] op_sel_hi:[1,0] neg_lo:[0,1] neg_hi:[0,1]
	v_pk_add_f32 v[30:31], v[30:31], v[22:23] op_sel_hi:[1,0] neg_lo:[0,1] neg_hi:[0,1]
	v_pk_mul_f32 v[32:33], v[28:29], v[28:29]
	v_pk_mul_f32 v[34:35], v[30:31], v[30:31]
	v_add_f32_e32 v22, v32, v33
	v_add_f32_e32 v22, v34, v22
	v_add_f32_e32 v22, v35, v22
	s_nop 1
	v_mov_b32_dpp v25, v22 quad_perm:[1,0,3,2] row_mask:0xf bank_mask:0xf
	v_mov_b64_e32 v[32:33], s[4:5]
	v_mad_i64_i32 v[32:33], s[0:1], v70, s7, v[32:33]
	s_waitcnt lgkmcnt(0)
	v_add_f32_e32 v22, v22, v25
	s_nop 1
	v_mov_b32_dpp v25, v22 quad_perm:[2,3,0,1] row_mask:0xf bank_mask:0xf
	s_waitcnt lgkmcnt(0)
	v_add_f32_e32 v22, v22, v25
	s_nop 1
	v_mov_b32_dpp v25, v22 row_half_mirror row_mask:0xf bank_mask:0xf
	s_waitcnt lgkmcnt(0)
	v_add_f32_e32 v25, v22, v25
	s_nop 1
	v_mov_b32_dpp v27, v25 row_mirror row_mask:0xf bank_mask:0xf
	v_mov_b32_e32 v99, 0x3727c5ac
	v_mov_b32_e32 v22, 0x260
	s_waitcnt lgkmcnt(0)
	v_add_f32_e32 v25, v25, v27
	v_mov_b32_e32 v27, v25
	s_nop 1
	v_permlane16_swap_b32_e32 v25, v27
	v_lshlrev_b32_e32 v0, 1, v1
	v_mov_b32_e32 v1, 0
	v_lshl_add_u64 v[32:33], v[32:33], 0, v[0:1]
	s_waitcnt lgkmcnt(0)
	v_add_f32_e32 v25, v25, v27
	v_fmamk_f32 v25, v25, 0x3c000000, v99
	v_mul_f32_e32 v27, 0x4f800000, v25
	v_cmp_gt_f32_e32 vcc, s8, v25
	s_nop 1
	v_cndmask_b32_e32 v25, v25, v27, vcc
	v_sqrt_f32_e32 v27, v25
	s_nop 0
	v_add_u32_e32 v34, -1, v27
	v_add_u32_e32 v35, 1, v27
	v_fma_f32 v36, -v34, v27, v25
	v_fma_f32 v37, -v35, v27, v25
	v_cmp_ge_f32_e64 s[0:1], 0, v36
	s_nop 1
	v_cndmask_b32_e64 v27, v27, v34, s[0:1]
	v_cmp_lt_f32_e64 s[0:1], 0, v37
	s_nop 1
	v_cndmask_b32_e64 v27, v27, v35, s[0:1]
	v_mul_f32_e32 v34, 0x37800000, v27
	v_cndmask_b32_e32 v27, v27, v34, vcc
	v_cmp_class_f32_e32 vcc, v25, v22
	s_nop 1
	v_cndmask_b32_e32 v25, v27, v25, vcc
	v_div_scale_f32 v27, s[0:1], v25, v25, 1.0
	v_rcp_f32_e32 v34, v27
	v_div_scale_f32 v0, vcc, 1.0, v25, 1.0
	v_fma_f32 v35, -v27, v34, 1.0
	v_fmac_f32_e32 v34, v35, v34
	v_mul_f32_e32 v35, v0, v34
	v_fma_f32 v36, -v27, v35, v0
	v_fmac_f32_e32 v35, v36, v34
	v_fma_f32 v0, -v27, v35, v0
	v_div_fmas_f32 v0, v0, v34, v35
	v_div_fixup_f32 v0, v0, v25, 1.0
	v_pk_mul_f32 v[28:29], v[28:29], v[0:1] op_sel_hi:[1,0]
	v_pk_mul_f32 v[30:31], v[30:31], v[0:1] op_sel_hi:[1,0]
	s_waitcnt vmcnt(0)
	v_pk_fma_f32 v[10:11], v[10:11], v[28:29], v[14:15]
	v_pk_fma_f32 v[12:13], v[12:13], v[30:31], v[16:17]
	v_cvt_pk_f16_f32 v10, v10, v11
	v_cvt_pk_f16_f32 v11, v12, v13
	s_andn2_b64 vcc, exec, s[2:3]
	global_store_dwordx2 v[32:33], v[10:11], off
	s_cbranch_vccnz .LBB5_225
	v_mad_u32_u24 v0, v75, s6, v72
	ds_read_b128 v[10:13], v0 offset:512
	s_waitcnt lgkmcnt(0)
	v_pk_add_f32 v[10:11], v[18:19], v[10:11]
	v_pk_add_f32 v[12:13], v[20:21], v[12:13]
	v_add_f32_e32 v0, v10, v11
	v_add_f32_e32 v0, v0, v12
	v_add_f32_e32 v0, v0, v13
	s_nop 1
	v_mov_b32_dpp v14, v0 quad_perm:[1,0,3,2] row_mask:0xf bank_mask:0xf
	s_waitcnt lgkmcnt(0)
	v_add_f32_e32 v0, v0, v14
	s_nop 1
	v_mov_b32_dpp v14, v0 quad_perm:[2,3,0,1] row_mask:0xf bank_mask:0xf
	s_waitcnt lgkmcnt(0)
	v_add_f32_e32 v0, v0, v14
	s_nop 1
	v_mov_b32_dpp v14, v0 row_half_mirror row_mask:0xf bank_mask:0xf
	s_waitcnt lgkmcnt(0)
	v_add_f32_e32 v0, v0, v14
	v_mul_f32_e32 v0, 0x3d000000, v0
	v_pk_add_f32 v[10:11], v[10:11], v[0:1] op_sel_hi:[1,0] neg_lo:[0,1] neg_hi:[0,1]
	v_pk_add_f32 v[12:13], v[12:13], v[0:1] op_sel_hi:[1,0] neg_lo:[0,1] neg_hi:[0,1]
	v_pk_mul_f32 v[14:15], v[10:11], v[10:11]
	v_pk_mul_f32 v[16:17], v[12:13], v[12:13]
	v_add_f32_e32 v0, v14, v15
	v_add_f32_e32 v0, v16, v0
	v_add_f32_e32 v0, v17, v0
	s_nop 1
	v_mov_b32_dpp v14, v0 quad_perm:[1,0,3,2] row_mask:0xf bank_mask:0xf
	s_waitcnt lgkmcnt(0)
	v_add_f32_e32 v0, v0, v14
	s_nop 1
	v_mov_b32_dpp v14, v0 quad_perm:[2,3,0,1] row_mask:0xf bank_mask:0xf
	s_waitcnt lgkmcnt(0)
	v_add_f32_e32 v0, v0, v14
	s_nop 1
	v_mov_b32_dpp v14, v0 row_half_mirror row_mask:0xf bank_mask:0xf
	s_waitcnt lgkmcnt(0)
	v_add_f32_e32 v0, v0, v14
	v_fmac_f32_e32 v99, 0x3d000000, v0
	v_mul_f32_e32 v0, 0x4f800000, v99
	v_cmp_gt_f32_e32 vcc, s8, v99
	v_mov_b64_e32 v[14:15], s[4:5]
	s_nop 0
	v_cndmask_b32_e32 v16, v99, v0, vcc
	v_sqrt_f32_e32 v17, v16
	v_lshlrev_b32_e32 v0, 1, v71
	v_add_u32_e32 v18, -1, v17
	v_add_u32_e32 v19, 1, v17
	v_fma_f32 v20, -v18, v17, v16
	v_fma_f32 v21, -v19, v17, v16
	v_cmp_ge_f32_e64 s[0:1], 0, v20
	s_nop 1
	v_cndmask_b32_e64 v17, v17, v18, s[0:1]
	v_cmp_lt_f32_e64 s[0:1], 0, v21
	s_nop 1
	v_cndmask_b32_e64 v17, v17, v19, s[0:1]
	v_mul_f32_e32 v18, 0x37800000, v17
	v_cndmask_b32_e32 v17, v17, v18, vcc
	v_cmp_class_f32_e32 vcc, v16, v22
	v_mad_i64_i32 v[14:15], s[0:1], v68, s7, v[14:15]
	s_nop 0
	v_cndmask_b32_e32 v16, v17, v16, vcc
	v_div_scale_f32 v17, s[0:1], v16, v16, 1.0
	v_rcp_f32_e32 v18, v17
	v_div_scale_f32 v19, vcc, 1.0, v16, 1.0
	v_lshl_add_u64 v[0:1], v[14:15], 0, v[0:1]
	v_fma_f32 v20, -v17, v18, 1.0
	v_fmac_f32_e32 v18, v20, v18
	v_mul_f32_e32 v20, v19, v18
	v_fma_f32 v21, -v17, v20, v19
	v_fmac_f32_e32 v20, v21, v18
	v_fma_f32 v17, -v17, v20, v19
	v_div_fmas_f32 v17, v17, v18, v20
	v_div_fixup_f32 v16, v17, v16, 1.0
	v_pk_mul_f32 v[10:11], v[10:11], v[16:17] op_sel_hi:[1,0]
	v_pk_mul_f32 v[12:13], v[12:13], v[16:17] op_sel_hi:[1,0]
	v_pk_fma_f32 v[2:3], v[2:3], v[10:11], v[6:7]
	v_pk_fma_f32 v[4:5], v[4:5], v[12:13], v[8:9]
	v_cvt_pk_f16_f32 v2, v2, v3
	v_cvt_pk_f16_f32 v3, v4, v5
	global_store_dwordx2 v[0:1], v[2:3], off offset:256

.LBB5_226:
	v_lshlrev_b32_e32 v99, 2, v76
	s_and_saveexec_b64 s[4:5], vcc
	s_cbranch_execz .LBB5_205
.LBB5_227:
	s_waitcnt vmcnt(12)
	ds_write_b128 v99, v[62:65] offset:10496
	s_or_b64 exec, exec, s[4:5]
	s_andn2_b64 vcc, exec, s[8:9]
	s_cbranch_vccz .LBB5_206
	s_branch .LBB5_207

	.amdhsa_kernel _Z8k_embed2PKfS0_S0_S0_S0_S0_S0_S0_S0_S0_PDF16_S0_S0_S0_S0_S0_S0_PDv8_DF16_
		.amdhsa_group_segment_fixed_size 21248
		.amdhsa_private_segment_fixed_size 0
		.amdhsa_kernarg_size 144
		.amdhsa_user_sgpr_count 2
		.amdhsa_user_sgpr_dispatch_ptr 0
		.amdhsa_user_sgpr_queue_ptr 0
		.amdhsa_user_sgpr_kernarg_segment_ptr 1
		.amdhsa_user_sgpr_dispatch_id 0
		.amdhsa_user_sgpr_kernarg_preload_length 0
		.amdhsa_user_sgpr_kernarg_preload_offset 0
		.amdhsa_user_sgpr_private_segment_size 0
		.amdhsa_uses_dynamic_stack 0
		.amdhsa_enable_private_segment 0
		.amdhsa_system_sgpr_workgroup_id_x 1
		.amdhsa_system_sgpr_workgroup_id_y 0
		.amdhsa_system_sgpr_workgroup_id_z 0
		.amdhsa_system_sgpr_workgroup_info 0
		.amdhsa_system_vgpr_workitem_id 0
		.amdhsa_next_free_vgpr 100
		.amdhsa_next_free_sgpr 31
		.amdhsa_accum_offset 100
		.amdhsa_reserve_vcc 1
		.amdhsa_float_round_mode_32 0
		.amdhsa_float_round_mode_16_64 0
		.amdhsa_float_denorm_mode_32 3
		.amdhsa_float_denorm_mode_16_64 3
		.amdhsa_dx10_clamp 1
		.amdhsa_ieee_mode 1
		.amdhsa_fp16_overflow 0
		.amdhsa_tg_split 0
		.amdhsa_exception_fp_ieee_invalid_op 0
		.amdhsa_exception_fp_denorm_src 0
		.amdhsa_exception_fp_ieee_div_zero 0
		.amdhsa_exception_fp_ieee_overflow 0
		.amdhsa_exception_fp_ieee_underflow 0
		.amdhsa_exception_fp_ieee_inexact 0
		.amdhsa_exception_int_div_zero 0
	.end_amdhsa_kernel

amdhsa.kernels:
  - .agpr_count:     0
    .args:
      - .actual_access:  read_only
        .address_space:  global
        .offset:         0
        .size:           8
        .value_kind:     global_buffer
      - .actual_access:  read_only
        .address_space:  global
        .offset:         8
        .size:           8
        .value_kind:     global_buffer
      - .actual_access:  read_only
        .address_space:  global
        .offset:         16
        .size:           8
        .value_kind:     global_buffer
      - .actual_access:  read_only
        .address_space:  global
        .offset:         24
        .size:           8
        .value_kind:     global_buffer
      - .actual_access:  read_only
        .address_space:  global
        .offset:         32
        .size:           8
        .value_kind:     global_buffer
      - .actual_access:  read_only
        .address_space:  global
        .offset:         40
        .size:           8
        .value_kind:     global_buffer
      - .actual_access:  read_only
        .address_space:  global
        .offset:         48
        .size:           8
        .value_kind:     global_buffer
      - .actual_access:  write_only
        .address_space:  global
        .offset:         56
        .size:           8
        .value_kind:     global_buffer
    .group_segment_fixed_size: 98304
    .kernarg_segment_align: 8
    .kernarg_segment_size: 64
    .language:       OpenCL C
    .language_version:
      - 2
      - 0
    .max_flat_workgroup_size: 512
    .name:           _Z11k_conv_mfmaPKDF16_PKDv8_DF16_PKfS5_S5_S5_S5_PDF16_
    .private_segment_fixed_size: 0
    .sgpr_count:     36
    .sgpr_spill_count: 0
    .symbol:         _Z11k_conv_mfmaPKDF16_PKDv8_DF16_PKfS5_S5_S5_S5_PDF16_.kd
    .uniform_work_group_size: 1
    .uses_dynamic_stack: false
    .vgpr_count:     173
    .vgpr_spill_count: 0
    .wavefront_size: 64
  - .agpr_count:     0
    .args:
      - .actual_access:  read_only
        .address_space:  global
        .offset:         0
        .size:           8
        .value_kind:     global_buffer
      - .actual_access:  read_only
        .address_space:  global
        .offset:         8
        .size:           8
        .value_kind:     global_buffer
      - .actual_access:  read_only
        .address_space:  global
        .offset:         16
        .size:           8
        .value_kind:     global_buffer
      - .actual_access:  write_only
        .address_space:  global
        .offset:         24
        .size:           8
        .value_kind:     global_buffer
    .group_segment_fixed_size: 25600
    .kernarg_segment_align: 8
    .kernarg_segment_size: 32
    .language:       OpenCL C
    .language_version:
      - 2
      - 0
    .max_flat_workgroup_size: 1024
    .name:           _Z12k_recon_mfmaPKDF16_PKDv8_DF16_PKfPf
    .private_segment_fixed_size: 0
    .sgpr_count:     25
    .sgpr_spill_count: 0
    .symbol:         _Z12k_recon_mfmaPKDF16_PKDv8_DF16_PKfPf.kd
    .uniform_work_group_size: 1
    .uses_dynamic_stack: false
    .vgpr_count:     84
    .vgpr_spill_count: 0
    .wavefront_size: 64
  - .agpr_count:     0
    .args:
      - .actual_access:  read_only
        .address_space:  global
        .offset:         0
        .size:           8
        .value_kind:     global_buffer
      - .actual_access:  read_only
        .address_space:  global
        .offset:         8
        .size:           8
        .value_kind:     global_buffer
      - .actual_access:  read_only
        .address_space:  global
        .offset:         16
        .size:           8
        .value_kind:     global_buffer
      - .actual_access:  write_only
        .address_space:  global
        .offset:         24
        .size:           8
        .value_kind:     global_buffer
      - .actual_access:  write_only
        .address_space:  global
        .offset:         32
        .size:           8
        .value_kind:     global_buffer
      - .actual_access:  write_only
        .address_space:  global
        .offset:         40
        .size:           8
        .value_kind:     global_buffer
      - .actual_access:  write_only
        .address_space:  global
        .offset:         48
        .size:           8
        .value_kind:     global_buffer
      - .actual_access:  write_only
        .address_space:  global
        .offset:         56
        .size:           8
        .value_kind:     global_buffer
      - .actual_access:  write_only
        .address_space:  global
        .offset:         64
        .size:           8
        .value_kind:     global_buffer
    .group_segment_fixed_size: 67600
    .kernarg_segment_align: 8
    .kernarg_segment_size: 72
    .language:       OpenCL C
    .language_version:
      - 2
      - 0
    .max_flat_workgroup_size: 512
    .name:           _Z11k_proj_mfmaPKDF16_PKDv8_DF16_PKfPfPS1_S6_PhS6_PDF16_
    .private_segment_fixed_size: 0
    .sgpr_count:     36
    .sgpr_spill_count: 0
    .symbol:         _Z11k_proj_mfmaPKDF16_PKDv8_DF16_PKfPfPS1_S6_PhS6_PDF16_.kd
    .uniform_work_group_size: 1
    .uses_dynamic_stack: false
    .vgpr_count:     155
    .vgpr_spill_count: 0
    .wavefront_size: 64
  - .agpr_count:     0
    .args:
      - .actual_access:  read_only
        .address_space:  global
        .offset:         0
        .size:           8
        .value_kind:     global_buffer
      - .actual_access:  read_only
        .address_space:  global
        .offset:         8
        .size:           8
        .value_kind:     global_buffer
      - .actual_access:  read_only
        .address_space:  global
        .offset:         16
        .size:           8
        .value_kind:     global_buffer
      - .actual_access:  read_only
        .address_space:  global
        .offset:         24
        .size:           8
        .value_kind:     global_buffer
      - .actual_access:  read_only
        .address_space:  global
        .offset:         32
        .size:           8
        .value_kind:     global_buffer
      - .actual_access:  read_only
        .address_space:  global
        .offset:         40
        .size:           8
        .value_kind:     global_buffer
      - .actual_access:  write_only
        .address_space:  global
        .offset:         48
        .size:           8
        .value_kind:     global_buffer
      - .actual_access:  write_only
        .address_space:  global
        .offset:         56
        .size:           8
        .value_kind:     global_buffer
      - .actual_access:  read_only
        .address_space:  global
        .offset:         64
        .size:           8
        .value_kind:     global_buffer
      - .actual_access:  read_only
        .address_space:  global
        .offset:         72
        .size:           8
        .value_kind:     global_buffer
      - .actual_access:  write_only
        .address_space:  global
        .offset:         80
        .size:           8
        .value_kind:     global_buffer
      - .actual_access:  write_only
        .address_space:  global
        .offset:         88
        .size:           8
        .value_kind:     global_buffer
    .group_segment_fixed_size: 65536
    .kernarg_segment_align: 8
    .kernarg_segment_size: 96
    .language:       OpenCL C
    .language_version:
      - 2
      - 0
    .max_flat_workgroup_size: 512
    .name:           _Z6k_attnPKDv8_DF16_PKfPKhS3_S3_S3_PfS6_S3_S3_PS_S7_
    .private_segment_fixed_size: 0
    .sgpr_count:     34
    .sgpr_spill_count: 0
    .symbol:         _Z6k_attnPKDv8_DF16_PKfPKhS3_S3_S3_PfS6_S3_S3_PS_S7_.kd
    .uniform_work_group_size: 1
    .uses_dynamic_stack: false
    .vgpr_count:     128
    .vgpr_spill_count: 0
    .wavefront_size: 64
  - .agpr_count:     8
    .args:
      - .actual_access:  read_only
        .address_space:  global
        .offset:         0
        .size:           8
        .value_kind:     global_buffer
      - .actual_access:  read_only
        .address_space:  global
        .offset:         8
        .size:           8
        .value_kind:     global_buffer
      - .actual_access:  read_only
        .address_space:  global
        .offset:         16
        .size:           8
        .value_kind:     global_buffer
      - .actual_access:  read_only
        .address_space:  global
        .offset:         24
        .size:           8
        .value_kind:     global_buffer
      - .actual_access:  read_only
        .address_space:  global
        .offset:         32
        .size:           8
        .value_kind:     global_buffer
      - .actual_access:  write_only
        .address_space:  global
        .offset:         40
        .size:           8
        .value_kind:     global_buffer
    .group_segment_fixed_size: 10560
    .kernarg_segment_align: 8
    .kernarg_segment_size: 48
    .language:       OpenCL C
    .language_version:
      - 2
      - 0
    .max_flat_workgroup_size: 256
    .name:           _Z8k_resid2PKDF16_PKfS0_S2_S2_PDF16_
    .private_segment_fixed_size: 0
    .sgpr_count:     38
    .sgpr_spill_count: 0
    .symbol:         _Z8k_resid2PKDF16_PKfS0_S2_S2_PDF16_.kd
    .uniform_work_group_size: 1
    .uses_dynamic_stack: false
    .vgpr_count:     120
    .vgpr_spill_count: 0
    .wavefront_size: 64
  - .agpr_count:     0
    .args:
      - .actual_access:  read_only
        .address_space:  global
        .offset:         0
        .size:           8
        .value_kind:     global_buffer
      - .actual_access:  read_only
        .address_space:  global
        .offset:         8
        .size:           8
        .value_kind:     global_buffer
      - .actual_access:  read_only
        .address_space:  global
        .offset:         16
        .size:           8
        .value_kind:     global_buffer
      - .actual_access:  read_only
        .address_space:  global
        .offset:         24
        .size:           8
        .value_kind:     global_buffer
      - .actual_access:  read_only
        .address_space:  global
        .offset:         32
        .size:           8
        .value_kind:     global_buffer
      - .actual_access:  read_only
        .address_space:  global
        .offset:         40
        .size:           8
        .value_kind:     global_buffer
      - .actual_access:  read_only
        .address_space:  global
        .offset:         48
        .size:           8
        .value_kind:     global_buffer
      - .actual_access:  read_only
        .address_space:  global
        .offset:         56
        .size:           8
        .value_kind:     global_buffer
      - .actual_access:  read_only
        .address_space:  global
        .offset:         64
        .size:           8
        .value_kind:     global_buffer
      - .actual_access:  read_only
        .address_space:  global
        .offset:         72
        .size:           8
        .value_kind:     global_buffer
      - .actual_access:  write_only
        .address_space:  global
        .offset:         80
        .size:           8
        .value_kind:     global_buffer
      - .actual_access:  read_only
        .address_space:  global
        .offset:         88
        .size:           8
        .value_kind:     global_buffer
      - .actual_access:  read_only
        .address_space:  global
        .offset:         96
        .size:           8
        .value_kind:     global_buffer
      - .actual_access:  read_only
        .address_space:  global
        .offset:         104
        .size:           8
        .value_kind:     global_buffer
      - .actual_access:  read_only
        .address_space:  global
        .offset:         112
        .size:           8
        .value_kind:     global_buffer
      - .actual_access:  read_only
        .address_space:  global
        .offset:         120
        .size:           8
        .value_kind:     global_buffer
      - .actual_access:  read_only
        .address_space:  global
        .offset:         128
        .size:           8
        .value_kind:     global_buffer
      - .actual_access:  write_only
        .address_space:  global
        .offset:         136
        .size:           8
        .value_kind:     global_buffer
    .group_segment_fixed_size: 21248
    .kernarg_segment_align: 8
    .kernarg_segment_size: 144
    .language:       OpenCL C
    .language_version:
      - 2
      - 0
    .max_flat_workgroup_size: 512
    .name:           _Z8k_embed2PKfS0_S0_S0_S0_S0_S0_S0_S0_S0_PDF16_S0_S0_S0_S0_S0_S0_PDv8_DF16_
    .private_segment_fixed_size: 0
    .sgpr_count:     37
    .sgpr_spill_count: 0
    .symbol:         _Z8k_embed2PKfS0_S0_S0_S0_S0_S0_S0_S0_S0_PDF16_S0_S0_S0_S0_S0_S0_PDv8_DF16_.kd
    .uniform_work_group_size: 1
    .uses_dynamic_stack: false
    .vgpr_count:     100
    .vgpr_spill_count: 0
    .wavefront_size: 64
